# P5b routed stream: per-unit accumulator zeroing (127 v_mov per unit) removed as well; every unit's first stage already overwrites the accumulators through the SrcC=0 body
# speedup vs baseline: 1.0174x; 1.0025x over previous
; __device__ void rt5b_stream(const Params& p, unsigned char* smem, const XMap& xm) {
;     ...
;     for (int i = 0; i < nmine; ++i) {
;         const bool wact = wr * 128 < nrow_c;
;         const bool have_n = i + 1 < nmine;
;         int sl00, sl01, sl10, sl11, sl20, sl21, sl30, sl31;
;         { const int rb_ = wr * 128 + (lane >> 2);
;           sl00 = rb_ < nrow_c ? lst_c[rb_] : -1; sl01 = rb_ + 16 < nrow_c ? lst_c[rb_ + 16] : -1; sl10 = rb_ + 32 < nrow_c ? lst_c[rb_ + 32] : -1; sl11 = rb_ + 48 < nrow_c ? lst_c[rb_ + 48] : -1;
;           sl20 = rb_ + 64 < nrow_c ? lst_c[rb_ + 64] : -1; sl21 = rb_ + 80 < nrow_c ? lst_c[rb_ + 80] : -1; sl30 = rb_ + 96 < nrow_c ? lst_c[rb_ + 96] : -1; sl31 = rb_ + 112 < nrow_c ? lst_c[rb_ + 112] : -1; }
; #pragma unroll
;         for (int m = 0; m < 8; ++m)
; #pragma unroll
;             for (int n = 0; n < 4; ++n) acc[m][n] = (f32x4){0.f, 0.f, 0.f, 0.f};
.LBB0_1179:
	s_or_b64 exec, exec, s[0:1]
	s_add_i32 s73, s73, 1
	v_cmp_lt_i32_e64 s[0:1], s66, v5
	s_cmp_lt_i32 s73, s3
	v_mov_b32_e32 v5, v131
	v_mov_b32_e32 v9, v131
	v_mov_b32_e32 v7, v131
	v_mov_b32_e32 v13, v131
	v_mov_b32_e32 v11, v131
	v_mov_b32_e32 v17, v131
	v_mov_b32_e32 v15, v131
	s_mul_i32 s75, s73, s64
	v_mov_b32_e32 v2, 0
	s_mov_b32 s74, 1
	s_cselect_b64 s[54:55], -1, 0
	s_waitcnt vmcnt(0)
	v_cmp_lt_i32_e64 s[6:7], -1, v130
	v_lshlrev_b64 v[152:153], 10, v[130:131]
	v_cmp_lt_i32_e64 s[8:9], -1, v4
	v_lshlrev_b64 v[154:155], 10, v[4:5]
	v_cmp_lt_i32_e64 s[10:11], -1, v8
	v_lshlrev_b64 v[156:157], 10, v[8:9]
	v_cmp_lt_i32_e64 s[12:13], -1, v6
	v_lshlrev_b64 v[158:159], 10, v[6:7]
	v_cmp_lt_i32_e64 s[14:15], -1, v12
	v_lshlrev_b64 v[160:161], 10, v[12:13]
	v_cmp_lt_i32_e64 s[16:17], -1, v10
	v_lshlrev_b64 v[162:163], 10, v[10:11]
	v_cmp_lt_i32_e64 s[18:19], -1, v16
	v_lshlrev_b64 v[164:165], 10, v[16:17]
	v_cmp_lt_i32_e64 s[20:21], -1, v14
	v_lshlrev_b64 v[166:167], 10, v[14:15]
	s_add_i32 s75, s75, s69
	s_movk_i32 s76, 0x4000
	s_mov_b32 s77, 0
	s_branch .LBB0_1183
